# O1/O3/FFN-down GEMM heads: compiler vmcnt(0) that only caught the stage-0 LDS-DMA requests removed, template vmcnt(2) governs (on top of quant sums-first)
# speedup vs baseline: 1.0059x; 1.0059x over previous
; #define PG8_STAGE(bufoff, gbase, voff) do { _Pragma("unroll") for (int _i = 0; _i < 2; ++_i) \
;         __builtin_amdgcn_global_load_lds((const unsigned*)((const char*)(gbase) + (voff)[_i]), (LAS unsigned*)(lds + (bufoff) + ldsw + _i * 8192), 16, 0, 0); } while (0)
; #define PG8_WAIT_V(n) asm volatile("s_waitcnt vmcnt(" #n ")" ::: "memory")
; #define PG8_BAR __builtin_amdgcn_s_barrier()
; template <class Epi, bool ALIGN_EPI, bool SP2>
; __device__ __forceinline__ void gemm_phase(LAS unsigned char* lds, LAS float* tab, const Gemm g, const StaticOrder& S, const Epi& E, int wave_s) {
;     ...
;     Unit cur, nxt; int ui = 0;
;     if (!S.next(0, cur)) return;
;     typedef typename Epi::AccV AccV; AccV acc[2][2][4][2];
; #pragma unroll
;     for (int a = 0; a < 2; ++a)
; #pragma unroll
;         for (int b = 0; b < 2; ++b)
; #pragma unroll
;             for (int m = 0; m < 4; ++m)
; #pragma unroll
;                 for (int n = 0; n < 2; ++n) acc[a][b][m][n] = AccV{};
;     bf16x8 At[4][2], B0[2][2], B1[2][2];
;     const char* cA = (const char*)g.A + (size_t)cur.pm * tstepA + (cur.hs > 0 ? hstepA : 0); const char* cB = (const char*)g.Bt + (size_t)cur.pn * tstepB;
;     if constexpr (SP2) {
;         PG8_STAGE(PG8_SB(0, 0), cB, voffB); PG8_STAGE(PG8_SB(0, 1), cB + hstepB, voffB); PG8_STAGE(PG8_SA(0, 0), cA, voffA); PG8_STAGE(PG8_SA(0, 1), cA + hstepA, voffA);
;         if (wr == 1) PG8_BAR;
;         PG8_WAIT_V(2); PG8_BAR;
;         PG8_STAGE(PG8_SB(1, 0), cB + kstep, voffB); PG8_STAGE(PG8_SA(1, 0), cA + kstep, voffA); PG8_STAGE(PG8_SB(1, 1), cB + hstepB + kstep, voffB);
;         PG8_WAIT_V(6); PG8_BAR;
.LBB0_280:
	s_add_u32 s39, s4, 0x8700000
	v_readlane_b32 s6, v255, 3
	s_addc_u32 s40, s5, 0
	s_mul_hi_u32 s3, s6, 0x3000
	s_mulk_i32 s6, 0x3000
	v_lshrrev_b32_e32 v19, 1, v2
	s_add_u32 s8, s4, s6
	v_and_b32_e32 v20, 24, v19
	s_addc_u32 s9, s5, s3
	v_and_b32_e32 v0, 15, v2
	v_lshlrev_b32_e32 v19, 1, v20
	s_lshl_b32 s1, s1, 5
	v_lshl_or_b32 v18, s2, 6, v0
	v_lshl_or_b32 v19, v0, 6, v19
	v_lshlrev_b32_e32 v0, 2, v0
	s_and_b32 s14, s1, 0x60
	s_add_i32 m0, s35, 0x18000
	v_lshl_add_u64 v[10:11], v[10:11], 0, s[90:91]
	s_lshl_b32 s2, s2, 13
	v_and_b32_e32 v21, 32, v0
	s_lshl_b32 s1, s14, 7
	s_waitcnt vmcnt(2)
	s_barrier
	global_load_lds_dwordx4 v[10:11], off
	v_lshl_add_u64 v[8:9], v[8:9], 0, s[90:91]
	s_add_i32 m0, s35, 0x1a000
	s_add_i32 s41, s35, 0x8000
	s_add_i32 s44, s35, 0xa000
	v_bitop3_b32 v22, v19, s2, v21 bitop3:0xde
	global_load_lds_dwordx4 v[8:9], off
	v_lshl_add_u64 v[4:5], v[4:5], 0, s[90:91]
	s_mov_b32 m0, s41
	s_add_u32 s2, s24, 0x20080
	global_load_lds_dwordx4 v[4:5], off
	v_lshl_add_u64 v[4:5], v[6:7], 0, s[90:91]
	s_mov_b32 m0, s44
	s_addc_u32 s3, s25, 0
	global_load_lds_dwordx4 v[4:5], off
	s_add_i32 m0, s35, 0x1c000
	v_lshl_add_u64 v[4:5], s[2:3], 0, v[134:135]
	global_load_lds_dwordx4 v[4:5], off
	v_lshl_add_u64 v[4:5], s[2:3], 0, v[130:131]
	s_add_i32 m0, s35, 0x1e000
	v_readlane_b32 s7, v255, 4
	global_load_lds_dwordx4 v[4:5], off
	v_bitop3_b32 v188, v19, s1, v21 bitop3:0xde
	s_movk_i32 s1, 0x100
	v_cmp_gt_i32_e64 s[6:7], s1, v2
	s_add_i32 s1, 0, 0x20000
	s_cmpk_lt_u32 s0, 0x100
	s_cselect_b64 s[12:13], -1, 0
	s_and_b32 s0, s0, 0xffffff00
	v_lshl_add_u32 v189, v2, 2, s1
	s_add_i32 s1, s1, s0
	v_ashrrev_i32_e32 v19, 31, v18
	v_lshl_add_u64 v[2:3], v[2:3], 2, s[4:5]
	s_mov_b64 s[2:3], 0xf800000
	v_add_u32_e32 v190, s1, v0
	v_lshlrev_b64 v[140:141], 11, v[18:19]
	s_mov_b64 s[0:1], 0x40000
	v_lshl_add_u64 v[138:139], v[2:3], 0, s[2:3]
	v_or_b32_e32 v2, 16, v18
	v_lshl_add_u64 v[148:149], v[140:141], 0, s[0:1]
	s_mov_b64 s[0:1], 0x48000
	v_ashrrev_i32_e32 v3, 31, v2
	v_lshl_add_u64 v[150:151], v[140:141], 0, s[0:1]
	s_mov_b64 s[0:1], 0x50000
	v_lshlrev_b64 v[142:143], 11, v[2:3]
	v_or_b32_e32 v2, 32, v18
	v_lshl_add_u64 v[152:153], v[140:141], 0, s[0:1]
	s_mov_b64 s[0:1], 0x58000
	v_ashrrev_i32_e32 v3, 31, v2
	v_lshl_add_u64 v[154:155], v[140:141], 0, s[0:1]
	s_lshl_b32 s0, s14, 2
	v_lshlrev_b64 v[144:145], 11, v[2:3]
	v_or_b32_e32 v2, 48, v18
	s_add_u32 s0, s8, s0
	v_ashrrev_i32_e32 v3, 31, v2
	s_addc_u32 s1, s9, 0
	v_lshlrev_b32_e32 v0, 2, v20
	v_lshlrev_b64 v[146:147], 11, v[2:3]
	v_lshl_add_u64 v[2:3], s[0:1], 0, v[0:1]
	v_lshlrev_b32_e32 v0, 13, v16
	s_mov_b64 s[0:1], 0x80000
	v_and_b32_e32 v0, 0xffffc000, v0
	v_lshl_add_u64 v[156:157], v[2:3], 0, s[0:1]
	v_lshl_add_u32 v0, v15, 10, v0
	v_and_b32_e32 v2, 1, v16
	v_lshl_or_b32 v0, v2, 6, v0
	v_lshl_add_u32 v158, v17, 1, v0
	v_lshlrev_b32_e32 v0, 13, v12
	v_and_b32_e32 v0, 0xffffc000, v0
	s_waitcnt vmcnt(6)
	v_lshl_add_u32 v0, v13, 10, v0
	v_and_b32_e32 v2, 1, v12
	v_lshl_or_b32 v0, v2, 6, v0
	v_mov_b32_e32 v159, v1
	v_lshl_add_u32 v160, v14, 1, v0
	v_mov_b32_e32 v161, v1
	s_mov_b32 s0, 0
	v_add_u32_e32 v191, 0, v22
	s_lshl_b32 s45, s14, 1
	v_lshlrev_b32_e32 v0, 1, v20
	v_readlane_b32 s1, v254, 30
	v_readlane_b32 s4, v254, 31
	s_barrier
	v_readlane_b32 s5, v254, 32
	s_branch .LBB0_283

; #define PG8_STAGE(bufoff, gbase, voff) do { _Pragma("unroll") for (int _i = 0; _i < 2; ++_i) \
;         __builtin_amdgcn_global_load_lds((const unsigned*)((const char*)(gbase) + (voff)[_i]), (LAS unsigned*)(lds + (bufoff) + ldsw + _i * 8192), 16, 0, 0); } while (0)
; #define PG8_WAIT_V(n) asm volatile("s_waitcnt vmcnt(" #n ")" ::: "memory")
; #define PG8_BAR __builtin_amdgcn_s_barrier()
; template <class Epi, bool ALIGN_EPI, bool SP2>
; __device__ __forceinline__ void gemm_phase(LAS unsigned char* lds, LAS float* tab, const Gemm g, const StaticOrder& S, const Epi& E, int wave_s) {
;     ...
;     const char* cA = (const char*)g.A + (size_t)cur.pm * tstepA + (cur.hs > 0 ? hstepA : 0); const char* cB = (const char*)g.Bt + (size_t)cur.pn * tstepB;
;     if constexpr (SP2) {
;         PG8_STAGE(PG8_SB(0, 0), cB, voffB); PG8_STAGE(PG8_SB(0, 1), cB + hstepB, voffB); PG8_STAGE(PG8_SA(0, 0), cA, voffA); PG8_STAGE(PG8_SA(0, 1), cA + hstepA, voffA);
;         if (wr == 1) PG8_BAR;
;         PG8_WAIT_V(2); PG8_BAR;
;         PG8_STAGE(PG8_SB(1, 0), cB + kstep, voffB); PG8_STAGE(PG8_SA(1, 0), cA + kstep, voffA); PG8_STAGE(PG8_SB(1, 1), cB + hstepB + kstep, voffB);
;         PG8_WAIT_V(6); PG8_BAR;
.LBB0_429:
	v_bfe_u32 v17, v16, 4, 2
	s_add_u32 s10, s6, 0x5e00000
	v_and_b32_e32 v18, 15, v16
	v_lshlrev_b32_e32 v20, 4, v17
	v_lshlrev_b32_e32 v16, 2, v16
	s_addc_u32 s11, s7, 0
	s_and_b32 s1, s1, 3
	s_lshl_b32 s4, s2, 6
	v_lshl_or_b32 v20, v18, 6, v20
	s_lshl_b32 s2, s2, 13
	v_and_b32_e32 v16, 32, v16
	s_add_i32 m0, s39, 0x18000
	v_lshl_add_u64 v[8:9], v[8:9], 0, s[90:91]
	v_bitop3_b32 v21, v20, s2, v16 bitop3:0xde
	s_lshl_b32 s2, s1, 12
	s_waitcnt vmcnt(2)
	s_barrier
	global_load_lds_dwordx4 v[8:9], off
	v_lshl_add_u64 v[6:7], v[6:7], 0, s[90:91]
	s_add_i32 m0, s39, 0x1a000
	s_add_i32 s43, s39, 0x8000
	s_add_i32 s44, s39, 0xa000
	v_bitop3_b32 v212, v20, s2, v16 bitop3:0xde
	global_load_lds_dwordx4 v[6:7], off
	v_lshl_add_u64 v[2:3], v[2:3], 0, s[90:91]
	s_mov_b32 m0, s43
	s_add_u32 s2, s28, 0x40080
	global_load_lds_dwordx4 v[2:3], off
	v_lshl_add_u64 v[2:3], v[4:5], 0, s[90:91]
	s_mov_b32 m0, s44
	s_addc_u32 s3, s29, 0
	global_load_lds_dwordx4 v[2:3], off
	s_add_i32 m0, s39, 0x1c000
	v_lshl_add_u64 v[2:3], s[2:3], 0, v[0:1]
	global_load_lds_dwordx4 v[2:3], off
	v_lshl_add_u64 v[2:3], s[2:3], 0, v[194:195]
	s_add_i32 m0, s39, 0x1e000
	s_cmpk_lt_u32 s0, 0x100
	global_load_lds_dwordx4 v[2:3], off
	v_lshlrev_b32_e32 v2, 14, v10
	v_and_b32_e32 v2, 0xffff8000, v2
	v_lshl_add_u32 v2, v11, 11, v2
	v_and_b32_e32 v3, 1, v10
	s_cselect_b64 s[12:13], -1, 0
	s_ashr_i32 s0, s4, 31
	v_lshl_or_b32 v2, v3, 6, v2
	v_mov_b32_e32 v197, s0
	s_lshl_b32 s0, s1, 2
	v_lshl_add_u32 v198, v12, 1, v2
	v_lshlrev_b32_e32 v2, 14, v13
	v_lshlrev_b32_e32 v19, 3, v17
	s_add_u32 s0, s6, s0
	v_and_b32_e32 v2, 0xffff8000, v2
	s_waitcnt vmcnt(6)
	v_lshl_or_b32 v213, s1, 5, v19
	s_addc_u32 s1, s7, 0
	v_lshl_add_u32 v2, v14, 11, v2
	v_and_b32_e32 v3, 1, v13
	s_add_u32 s46, s0, 0x7e00000
	v_lshl_or_b32 v2, v3, 6, v2
	v_or_b32_e32 v196, s4, v18
	s_mov_b32 s45, 0
	v_cmp_eq_u32_e64 s[4:5], 0, v17
	s_addc_u32 s47, s1, 0
	v_mov_b32_e32 v199, v1
	v_lshl_add_u32 v200, v15, 1, v2
	v_mov_b32_e32 v201, v1
	v_add_u32_e32 v214, 0, v21
	s_barrier
	s_branch .LBB0_432

; #define PG8_STAGE(bufoff, gbase, voff) do { _Pragma("unroll") for (int _i = 0; _i < 2; ++_i) \
;         __builtin_amdgcn_global_load_lds((const unsigned*)((const char*)(gbase) + (voff)[_i]), (LAS unsigned*)(lds + (bufoff) + ldsw + _i * 8192), 16, 0, 0); } while (0)
; #define PG8_WAIT_V(n) asm volatile("s_waitcnt vmcnt(" #n ")" ::: "memory")
; #define PG8_BAR __builtin_amdgcn_s_barrier()
; template <class Epi, bool ALIGN_EPI, bool SP2>
; __device__ __forceinline__ void gemm_phase(LAS unsigned char* lds, LAS float* tab, const Gemm g, const StaticOrder& S, const Epi& E, int wave_s) {
;     ...
;     const char* cA = (const char*)g.A + (size_t)cur.pm * tstepA + (cur.hs > 0 ? hstepA : 0); const char* cB = (const char*)g.Bt + (size_t)cur.pn * tstepB;
;     if constexpr (SP2) {
;         PG8_STAGE(PG8_SB(0, 0), cB, voffB); PG8_STAGE(PG8_SB(0, 1), cB + hstepB, voffB); PG8_STAGE(PG8_SA(0, 0), cA, voffA); PG8_STAGE(PG8_SA(0, 1), cA + hstepA, voffA);
;         if (wr == 1) PG8_BAR;
;         PG8_WAIT_V(2); PG8_BAR;
;         PG8_STAGE(PG8_SB(1, 0), cB + kstep, voffB); PG8_STAGE(PG8_SA(1, 0), cA + kstep, voffA); PG8_STAGE(PG8_SB(1, 1), cB + hstepB + kstep, voffB);
;         PG8_WAIT_V(6); PG8_BAR;
.LBB0_2168:
	s_and_b64 s[10:11], s[14:15], exec
	s_cselect_b32 s19, s7, 0
	s_cselect_b32 s18, s6, 0
	s_add_u32 s20, s8, 0x5e00000
	s_addc_u32 s21, s9, 0
	s_cmp_eq_u64 s[18:19], 0
	v_bfe_u32 v19, v18, 4, 2
	s_cselect_b64 s[22:23], -1, 0
	s_cmp_lg_u64 s[18:19], 0
	v_and_b32_e32 v20, 15, v18
	v_lshlrev_b32_e32 v22, 4, v19
	v_lshlrev_b32_e32 v18, 2, v18
	s_cselect_b64 s[24:25], -1, 0
	s_and_b32 s1, s1, 3
	s_lshl_b32 s10, s3, 6
	v_lshl_or_b32 v22, v20, 6, v22
	s_lshl_b32 s3, s3, 13
	v_and_b32_e32 v18, 32, v18
	s_add_i32 m0, s45, 0x18000
	v_lshl_add_u64 v[8:9], v[8:9], 0, s[90:91]
	v_bitop3_b32 v23, v22, s3, v18 bitop3:0xde
	s_lshl_b32 s3, s1, 12
	s_waitcnt vmcnt(2)
	s_barrier
	global_load_lds_dwordx4 v[8:9], off
	v_lshl_add_u64 v[6:7], v[6:7], 0, s[90:91]
	s_add_i32 m0, s45, 0x1a000
	s_add_i32 s50, s45, 0x8000
	s_add_i32 s51, s45, 0xa000
	global_load_lds_dwordx4 v[6:7], off
	v_lshl_add_u64 v[2:3], v[2:3], 0, s[90:91]
	s_mov_b32 m0, s50
	s_add_u32 s6, s36, 0xb0080
	global_load_lds_dwordx4 v[2:3], off
	v_lshl_add_u64 v[2:3], v[4:5], 0, s[90:91]
	s_mov_b32 m0, s51
	s_addc_u32 s7, s37, 0
	global_load_lds_dwordx4 v[2:3], off
	s_add_i32 m0, s45, 0x1c000
	v_lshl_add_u64 v[2:3], s[6:7], 0, v[0:1]
	global_load_lds_dwordx4 v[2:3], off
	v_lshl_add_u64 v[2:3], s[6:7], 0, v[194:195]
	s_add_i32 m0, s45, 0x1e000
	s_cmpk_lt_u32 s0, 0x100
	global_load_lds_dwordx4 v[2:3], off
	s_cselect_b64 s[26:27], -1, 0
	s_ashr_i32 s0, s10, 31
	v_mov_b32_e32 v197, s0
	s_lshl_b32 s0, s1, 2
	v_lshlrev_b32_e32 v21, 3, v19
	s_add_u32 s0, s8, s0
	v_bitop3_b32 v216, v22, s3, v18 bitop3:0xde
	v_lshl_or_b32 v217, s1, 5, v21
	s_addc_u32 s1, s9, 0
	s_movk_i32 s3, 0xb00
	s_add_u32 s55, s0, 0x7e00000
	v_lshrrev_b32_e32 v3, 1, v10
	v_mul_lo_u32 v2, v12, s3
	s_mov_b32 s8, 0xb000
	s_addc_u32 s56, s1, 0
	v_mad_u64_u32 v[2:3], s[0:1], v3, s8, v[2:3]
	v_or_b32_e32 v2, v2, v11
	v_or_b32_e32 v196, s10, v20
	v_add_lshl_u32 v2, v2, v13, 1
	v_mov_b32_e32 v3, v1
	s_mov_b64 s[10:11], 0xb0080
	v_lshl_add_u64 v[198:199], v[2:3], 0, s[10:11]
	v_lshrrev_b32_e32 v3, 1, v14
	v_mul_lo_u32 v2, v16, s3
	v_mad_u64_u32 v[2:3], s[0:1], v3, s8, v[2:3]
	s_waitcnt vmcnt(6)
	v_or_b32_e32 v2, v2, v15
	v_add_lshl_u32 v2, v2, v17, 1
	v_mov_b32_e32 v3, v1
	s_mov_b32 s49, 0
	v_cmp_eq_u32_e64 s[6:7], 0, v19
	v_lshl_add_u64 v[200:201], v[2:3], 0, s[10:11]
	v_add_u32_e32 v218, 0, v23
	s_barrier
	s_branch .LBB0_2171
